# v032 + attention block-top wait relaxed to vmcnt(9) (does not wait for the just-issued (max,sum) store)
# baseline (speedup 1.0000x reference)
.LBB0_1076:
	s_add_i32 s6, s12, 0xffffff80
	s_and_b32 s6, s6, 0x80
	v_or_b32_e32 v2, s6, v153
	v_lshl_or_b32 v2, v2, 8, v170
	v_add_u32_e32 v3, 0, v2
	v_add_u32_e32 v2, s88, v2
	s_waitcnt vmcnt(9)
	s_barrier
	ds_write_b128 v2, v[18:21]
	v_or_b32_e32 v2, s6, v171
	v_lshl_or_b32 v2, v2, 8, v172
	ds_write_b128 v3, v[34:37]
	v_add_u32_e32 v3, 0, v2
	v_add_u32_e32 v2, s88, v2
	ds_write_b128 v2, v[22:25]
	v_or_b32_e32 v2, s6, v173
	v_lshl_or_b32 v2, v2, 8, v170
	ds_write_b128 v3, v[38:41]
	v_add_u32_e32 v3, 0, v2
	v_add_u32_e32 v2, s88, v2
	ds_write_b128 v2, v[26:29]
	v_or_b32_e32 v2, s6, v174
	v_lshlrev_b32_e32 v2, 8, v2
	s_add_i32 s51, s2, 1
	v_lshl_or_b32 v2, v178, 4, v2
	s_cmp_lt_i32 s51, s59
	ds_write_b128 v3, v[42:45]
	v_add_u32_e32 v3, 0, v2
	v_add_u32_e32 v2, s88, v2
	s_cselect_b64 s[54:55], -1, 0
	s_cmp_ge_i32 s51, s59
	s_mov_b64 s[6:7], -1
	ds_write_b128 v3, v[46:49]
	ds_write_b128 v2, v[30:33]
	s_waitcnt lgkmcnt(0)
	s_barrier
	s_cbranch_scc0 .LBB0_1086
	s_and_b64 vcc, exec, s[4:5]
	s_mov_b32 s40, s56
	s_mov_b32 s44, s57
	s_mov_b32 s50, s97
	s_mov_b32 s41, s33
	s_mov_b32 s23, s58
	s_mov_b32 s61, s10
	s_cbranch_vccnz .LBB0_1085
	v_cndmask_b32_e64 v2, 0, 1, s[24:25]
	v_cmp_ne_u32_e64 s[6:7], 1, v2
	s_andn2_b64 vcc, exec, s[24:25]
	s_cbranch_vccnz .LBB0_1102
	global_load_dwordx4 v[34:37], v[130:131], off offset:2048
	global_load_dwordx4 v[2:5], v[132:133], off
	global_load_dwordx4 v[38:41], v[134:135], off offset:2048
	global_load_dwordx4 v[6:9], v[136:137], off
	s_cbranch_execnz .LBB0_1081
